# speedup vs baseline: 1.0033x; 1.0033x over previous
.LBB2_2:
	s_waitcnt vmcnt(2)
	v_lshlrev_b32_e32 v27, 3, v6
	v_lshlrev_b32_e32 v28, 3, v7
	v_lshlrev_b32_e32 v29, 3, v8
	s_waitcnt vmcnt(0)
	v_lshlrev_b32_e32 v30, 3, v11
	global_load_dwordx4 v[2:5], v[14:15], off
	v_and_or_b32 v27, v27, s10, v17
	v_and_or_b32 v28, v28, s10, v17
	v_and_or_b32 v29, v29, s10, v17
	v_and_or_b32 v30, v30, s10, v17
	v_lshlrev_b32_e32 v27, 4, v27
	v_lshlrev_b32_e32 v44, 4, v28
	v_lshlrev_b32_e32 v45, 4, v29
	v_lshlrev_b32_e32 v46, 4, v30
	global_load_dwordx4 v[28:31], v27, s[4:5] sc1
	global_load_dwordx4 v[32:35], v44, s[4:5] sc1
	global_load_dwordx4 v[36:39], v45, s[4:5] sc1
	global_load_dwordx4 v[40:43], v46, s[4:5] sc1
	v_mov_b32_e32 v27, v12
	v_and_b32_sdwa v6, v6, v9 dst_sel:DWORD dst_unused:UNUSED_PAD src0_sel:WORD_1 src1_sel:DWORD
	v_and_b32_sdwa v7, v7, v9 dst_sel:DWORD dst_unused:UNUSED_PAD src0_sel:WORD_1 src1_sel:DWORD
	v_and_b32_sdwa v8, v8, v9 dst_sel:DWORD dst_unused:UNUSED_PAD src0_sel:WORD_1 src1_sel:DWORD
	v_and_b32_sdwa v11, v11, v9 dst_sel:DWORD dst_unused:UNUSED_PAD src0_sel:WORD_1 src1_sel:DWORD
	v_cvt_f32_f16_e32 v44, v6
	v_add_u32_e32 v6, 8, v27
	v_cvt_f32_f16_e32 v45, v7
	v_cvt_f32_f16_e32 v46, v8
	v_cvt_f32_f16_e32 v47, v11
	v_cmp_gt_i32_e32 vcc, v6, v13
	v_lshl_add_u64 v[14:15], v[14:15], 0, 16
	v_add_u32_e32 v12, 4, v27
	s_or_b64 s[8:9], vcc, s[8:9]
	s_waitcnt vmcnt(3)
	v_fma_mix_f32 v19, v28, v44, v19 op_sel:[0,0,0] op_sel_hi:[1,0,0]
	v_fma_mix_f32 v20, v28, v44, v20 op_sel:[1,0,0] op_sel_hi:[1,0,0]
	v_fma_mix_f32 v21, v29, v44, v21 op_sel:[0,0,0] op_sel_hi:[1,0,0]
	v_fma_mix_f32 v22, v29, v44, v22 op_sel:[1,0,0] op_sel_hi:[1,0,0]
	v_fma_mix_f32 v23, v30, v44, v23 op_sel:[0,0,0] op_sel_hi:[1,0,0]
	v_fma_mix_f32 v24, v30, v44, v24 op_sel:[1,0,0] op_sel_hi:[1,0,0]
	v_fma_mix_f32 v25, v31, v44, v25 op_sel:[0,0,0] op_sel_hi:[1,0,0]
	v_fma_mix_f32 v26, v31, v44, v26 op_sel:[1,0,0] op_sel_hi:[1,0,0]
	v_mov_b32_e32 v11, v5
	v_mov_b32_e32 v6, v2
	v_mov_b32_e32 v8, v4
	s_waitcnt vmcnt(2)
	v_fma_mix_f32 v19, v32, v45, v19 op_sel:[0,0,0] op_sel_hi:[1,0,0]
	v_fma_mix_f32 v20, v32, v45, v20 op_sel:[1,0,0] op_sel_hi:[1,0,0]
	v_fma_mix_f32 v21, v33, v45, v21 op_sel:[0,0,0] op_sel_hi:[1,0,0]
	v_fma_mix_f32 v22, v33, v45, v22 op_sel:[1,0,0] op_sel_hi:[1,0,0]
	v_fma_mix_f32 v23, v34, v45, v23 op_sel:[0,0,0] op_sel_hi:[1,0,0]
	v_fma_mix_f32 v24, v34, v45, v24 op_sel:[1,0,0] op_sel_hi:[1,0,0]
	v_fma_mix_f32 v25, v35, v45, v25 op_sel:[0,0,0] op_sel_hi:[1,0,0]
	v_fma_mix_f32 v26, v35, v45, v26 op_sel:[1,0,0] op_sel_hi:[1,0,0]
	s_nop 0
	v_mov_b32_e32 v7, v3
	s_waitcnt vmcnt(1)
	v_fma_mix_f32 v19, v36, v46, v19 op_sel:[0,0,0] op_sel_hi:[1,0,0]
	v_fma_mix_f32 v20, v36, v46, v20 op_sel:[1,0,0] op_sel_hi:[1,0,0]
	v_fma_mix_f32 v21, v37, v46, v21 op_sel:[0,0,0] op_sel_hi:[1,0,0]
	v_fma_mix_f32 v22, v37, v46, v22 op_sel:[1,0,0] op_sel_hi:[1,0,0]
	v_fma_mix_f32 v23, v38, v46, v23 op_sel:[0,0,0] op_sel_hi:[1,0,0]
	v_fma_mix_f32 v24, v38, v46, v24 op_sel:[1,0,0] op_sel_hi:[1,0,0]
	v_fma_mix_f32 v25, v39, v46, v25 op_sel:[0,0,0] op_sel_hi:[1,0,0]
	v_fma_mix_f32 v26, v39, v46, v26 op_sel:[1,0,0] op_sel_hi:[1,0,0]
	s_waitcnt vmcnt(0)
	v_fma_mix_f32 v19, v40, v47, v19 op_sel:[0,0,0] op_sel_hi:[1,0,0]
	v_fma_mix_f32 v20, v40, v47, v20 op_sel:[1,0,0] op_sel_hi:[1,0,0]
	v_fma_mix_f32 v21, v41, v47, v21 op_sel:[0,0,0] op_sel_hi:[1,0,0]
	v_fma_mix_f32 v22, v41, v47, v22 op_sel:[1,0,0] op_sel_hi:[1,0,0]
	v_fma_mix_f32 v23, v42, v47, v23 op_sel:[0,0,0] op_sel_hi:[1,0,0]
	v_fma_mix_f32 v24, v42, v47, v24 op_sel:[1,0,0] op_sel_hi:[1,0,0]
	v_fma_mix_f32 v25, v43, v47, v25 op_sel:[0,0,0] op_sel_hi:[1,0,0]
	v_fma_mix_f32 v26, v43, v47, v26 op_sel:[1,0,0] op_sel_hi:[1,0,0]
	s_andn2_b64 exec, exec, s[8:9]
	s_cbranch_execnz .LBB2_2
	s_or_b64 exec, exec, s[8:9]
	v_mov_b32_e32 v7, v3

.LBB3_2:
	s_waitcnt vmcnt(2)
	v_lshlrev_b32_e32 v26, 3, v0
	v_lshlrev_b32_e32 v27, 3, v1
	v_lshlrev_b32_e32 v28, 3, v2
	s_waitcnt vmcnt(0)
	v_lshlrev_b32_e32 v29, 3, v9
	global_load_dwordx4 v[22:25], v[20:21], off
	v_and_or_b32 v26, v26, s8, v3
	v_and_or_b32 v27, v27, s8, v3
	v_and_or_b32 v28, v28, s8, v3
	v_and_or_b32 v29, v29, s8, v3
	v_lshlrev_b32_e32 v42, 4, v26
	v_lshlrev_b32_e32 v43, 4, v27
	v_lshlrev_b32_e32 v44, 4, v28
	v_lshlrev_b32_e32 v45, 4, v29
	global_load_dwordx4 v[26:29], v42, s[4:5] sc1
	global_load_dwordx4 v[30:33], v43, s[4:5] sc1
	global_load_dwordx4 v[34:37], v44, s[4:5] sc1
	global_load_dwordx4 v[38:41], v45, s[4:5] sc1
	v_mov_b32_e32 v42, v18
	v_and_b32_sdwa v0, v0, v7 dst_sel:DWORD dst_unused:UNUSED_PAD src0_sel:WORD_1 src1_sel:DWORD
	v_and_b32_sdwa v1, v1, v7 dst_sel:DWORD dst_unused:UNUSED_PAD src0_sel:WORD_1 src1_sel:DWORD
	v_and_b32_sdwa v2, v2, v7 dst_sel:DWORD dst_unused:UNUSED_PAD src0_sel:WORD_1 src1_sel:DWORD
	v_cvt_f32_f16_e32 v43, v0
	v_add_u32_e32 v0, 8, v42
	v_and_b32_sdwa v9, v9, v7 dst_sel:DWORD dst_unused:UNUSED_PAD src0_sel:WORD_1 src1_sel:DWORD
	v_cvt_f32_f16_e32 v44, v1
	v_cvt_f32_f16_e32 v45, v2
	v_cmp_gt_i32_e32 vcc, v0, v19
	v_lshl_add_u64 v[20:21], v[20:21], 0, 16
	v_cvt_f32_f16_e32 v46, v9
	v_add_u32_e32 v18, 4, v42
	s_or_b64 s[6:7], vcc, s[6:7]
	s_waitcnt vmcnt(3)
	v_fma_mix_f32 v16, v26, v43, v16 op_sel:[0,0,0] op_sel_hi:[1,0,0]
	v_fma_mix_f32 v17, v26, v43, v17 op_sel:[1,0,0] op_sel_hi:[1,0,0]
	v_fma_mix_f32 v14, v27, v43, v14 op_sel:[0,0,0] op_sel_hi:[1,0,0]
	v_fma_mix_f32 v15, v27, v43, v15 op_sel:[1,0,0] op_sel_hi:[1,0,0]
	v_fma_mix_f32 v12, v28, v43, v12 op_sel:[0,0,0] op_sel_hi:[1,0,0]
	v_fma_mix_f32 v13, v28, v43, v13 op_sel:[1,0,0] op_sel_hi:[1,0,0]
	v_fma_mix_f32 v10, v29, v43, v10 op_sel:[0,0,0] op_sel_hi:[1,0,0]
	v_fma_mix_f32 v11, v29, v43, v11 op_sel:[1,0,0] op_sel_hi:[1,0,0]
	v_mov_b32_e32 v0, v22
	v_mov_b32_e32 v2, v24
	v_mov_b32_e32 v1, v23
	s_waitcnt vmcnt(2)
	v_fma_mix_f32 v16, v30, v44, v16 op_sel:[0,0,0] op_sel_hi:[1,0,0]
	v_fma_mix_f32 v17, v30, v44, v17 op_sel:[1,0,0] op_sel_hi:[1,0,0]
	v_fma_mix_f32 v14, v31, v44, v14 op_sel:[0,0,0] op_sel_hi:[1,0,0]
	v_fma_mix_f32 v15, v31, v44, v15 op_sel:[1,0,0] op_sel_hi:[1,0,0]
	v_fma_mix_f32 v12, v32, v44, v12 op_sel:[0,0,0] op_sel_hi:[1,0,0]
	v_fma_mix_f32 v13, v32, v44, v13 op_sel:[1,0,0] op_sel_hi:[1,0,0]
	v_fma_mix_f32 v10, v33, v44, v10 op_sel:[0,0,0] op_sel_hi:[1,0,0]
	v_fma_mix_f32 v11, v33, v44, v11 op_sel:[1,0,0] op_sel_hi:[1,0,0]
	s_waitcnt vmcnt(1)
	v_fma_mix_f32 v16, v34, v45, v16 op_sel:[0,0,0] op_sel_hi:[1,0,0]
	v_fma_mix_f32 v17, v34, v45, v17 op_sel:[1,0,0] op_sel_hi:[1,0,0]
	v_fma_mix_f32 v14, v35, v45, v14 op_sel:[0,0,0] op_sel_hi:[1,0,0]
	v_fma_mix_f32 v15, v35, v45, v15 op_sel:[1,0,0] op_sel_hi:[1,0,0]
	v_fma_mix_f32 v12, v36, v45, v12 op_sel:[0,0,0] op_sel_hi:[1,0,0]
	v_mov_b32_e32 v9, v25
	v_fma_mix_f32 v13, v36, v45, v13 op_sel:[1,0,0] op_sel_hi:[1,0,0]
	v_fma_mix_f32 v10, v37, v45, v10 op_sel:[0,0,0] op_sel_hi:[1,0,0]
	v_fma_mix_f32 v11, v37, v45, v11 op_sel:[1,0,0] op_sel_hi:[1,0,0]
	s_waitcnt vmcnt(0)
	v_fma_mix_f32 v16, v38, v46, v16 op_sel:[0,0,0] op_sel_hi:[1,0,0]
	v_fma_mix_f32 v17, v38, v46, v17 op_sel:[1,0,0] op_sel_hi:[1,0,0]
	v_fma_mix_f32 v14, v39, v46, v14 op_sel:[0,0,0] op_sel_hi:[1,0,0]
	v_fma_mix_f32 v15, v39, v46, v15 op_sel:[1,0,0] op_sel_hi:[1,0,0]
	v_fma_mix_f32 v12, v40, v46, v12 op_sel:[0,0,0] op_sel_hi:[1,0,0]
	v_fma_mix_f32 v13, v40, v46, v13 op_sel:[1,0,0] op_sel_hi:[1,0,0]
	v_fma_mix_f32 v10, v41, v46, v10 op_sel:[0,0,0] op_sel_hi:[1,0,0]
	v_fma_mix_f32 v11, v41, v46, v11 op_sel:[1,0,0] op_sel_hi:[1,0,0]
	s_andn2_b64 exec, exec, s[6:7]
	s_cbranch_execnz .LBB3_2
	s_or_b64 exec, exec, s[6:7]
